# baseline (speedup 1.0000x reference)
_Z19trunk_global_kernelPKfPKDF16_PDF16_S0_S2_S0_S0_PfS4_S0_S0_:
	s_load_dwordx8 s[16:23], s[0:1], 0x0
	s_load_dwordx8 s[8:15], s[0:1], 0x20
	s_lshl_b32 s3, s2, 4
	s_and_b32 s28, s3, 0xffffffe0
	v_lshrrev_b32_e32 v25, 7, v0
	v_lshlrev_b32_e32 v18, 4, v0
	v_or_b32_e32 v1, s28, v25
	v_and_b32_e32 v46, 0x7f0, v18
	v_mov_b32_e32 v47, 0
	v_lshlrev_b32_e32 v2, 9, v1
	s_waitcnt lgkmcnt(0)
	v_lshl_add_u64 v[10:11], s[16:17], 0, v[46:47]
	v_ashrrev_i32_e32 v3, 31, v2
	v_lshl_add_u64 v[12:13], v[2:3], 2, v[10:11]
	v_or_b32_e32 v2, 0x1000, v2
	v_or_b32_e32 v1, s3, v25
	s_and_b32 s30, s2, 1
	v_ashrrev_i32_e32 v3, 31, v2
	v_lshlrev_b32_e32 v1, 9, v1
	v_lshl_add_u64 v[14:15], v[2:3], 2, v[10:11]
	global_load_dwordx4 v[6:9], v[12:13], off nt
	global_load_dwordx4 v[2:5], v[14:15], off nt
	v_or_b32_e32 v12, 0x2000, v1
	s_mul_i32 s3, s30, 0x12980
	v_ashrrev_i32_e32 v13, 31, v12
	s_add_u32 s4, s8, s3
	v_lshrrev_b32_e32 v24, 6, v0
	v_lshl_add_u64 v[20:21], v[12:13], 2, v[10:11]
	v_or_b32_e32 v12, 0x3000, v1
	s_addc_u32 s5, s9, 0
	s_lshl_b32 s3, s2, 3
	v_ashrrev_i32_e32 v13, 31, v12
	v_and_b32_e32 v85, 63, v0
	v_and_or_b32 v82, s3, -16, v24
	v_lshl_add_u64 v[22:23], v[12:13], 2, v[10:11]
	global_load_dwordx4 v[14:17], v[20:21], off nt
	global_load_dwordx4 v[10:13], v[22:23], off nt
	v_lshl_or_b32 v20, v82, 8, v85
	v_ashrrev_i32_e32 v21, 31, v20
	v_lshl_add_u64 v[20:21], v[20:21], 2, s[22:23]
	v_lshlrev_b32_e32 v46, 4, v85
	global_load_dword v81, v[20:21], off
	global_load_dword v80, v[20:21], off offset:256
	global_load_dword v79, v[20:21], off offset:512
	global_load_dword v78, v[20:21], off offset:768
	v_lshl_add_u64 v[20:21], s[4:5], 0, v[46:47]
	s_mov_b32 s3, 0x10000
	s_mov_b64 s[6:7], 0x10980
	v_add_co_u32_e32 v26, vcc, s3, v20
	v_lshl_add_u64 v[22:23], v[20:21], 0, s[6:7]
	s_nop 0
	v_addc_co_u32_e32 v27, vcc, 0, v21, vcc
	s_mov_b32 s3, 0x11000
	global_load_dwordx4 v[74:77], v[22:23], off offset:1024
	global_load_dwordx4 v[70:73], v[22:23], off offset:2048
	global_load_dwordx4 v[34:37], v[26:27], off offset:2432
	global_load_dwordx4 v[62:65], v[22:23], off offset:3072
	v_add_co_u32_e32 v22, vcc, s3, v20
	s_mov_b32 s3, 0x12000
	s_nop 0
	v_addc_co_u32_e32 v23, vcc, 0, v21, vcc
	v_add_co_u32_e32 v20, vcc, s3, v20
	global_load_dwordx4 v[66:69], v[22:23], off offset:2432
	global_load_dwordx4 v[58:61], v[22:23], off offset:3456
	v_addc_co_u32_e32 v21, vcc, 0, v21, vcc
	global_load_dwordx4 v[54:57], v[20:21], off offset:384
	global_load_dwordx4 v[50:53], v[20:21], off offset:1408
	s_load_dwordx2 s[8:9], s[0:1], 0x50
	s_load_dwordx4 s[24:27], s[0:1], 0x40
	v_mov_b32_e32 v19, v47
	s_bitcmp1_b32 s2, 0
	v_lshl_add_u64 v[20:21], s[4:5], 0, v[18:19]
	s_mov_b64 s[0:1], 0x9500
	v_lshlrev_b32_e32 v22, 3, v85
	v_or_b32_e32 v1, 0xfffffc00, v0
	s_cselect_b64 s[6:7], -1, 0
	v_lshl_add_u64 v[20:21], v[20:21], 0, s[0:1]
	s_mov_b64 s[0:1], 0
	s_mov_b64 s[2:3], 0x4000
	s_movk_i32 s16, 0x2ff
	v_readfirstlane_b32 s44, v24
	s_lshl_b32 s45, s44, 10
	s_mov_b32 m0, s45
	s_nop 0
	global_load_lds_dwordx4 v[20:21], off
	v_lshl_add_u64 v[20:21], v[20:21], 0, s[2:3]
	s_cmp_lt_u32 s44, 12
	s_cbranch_scc0 .Lstage_skip1
	s_add_u32 s45, s45, 0x4000
	s_mov_b32 m0, s45
	s_nop 0
	global_load_lds_dwordx4 v[20:21], off
.Lstage_skip1:
	s_waitcnt vmcnt(0)
	v_mul_u32_u24_e32 v1, 0x1880, v24
	s_movk_i32 s0, 0x7000
	v_mov_b32_e32 v18, 0
	v_or_b32_e32 v23, 0xffffffc0, v85
	v_add3_u32 v26, v1, v46, s0
	s_mov_b64 s[0:1], 0
	v_mov_b32_e32 v19, v18
	v_mov_b32_e32 v20, v18
	v_mov_b32_e32 v21, v18
	s_movk_i32 s2, 0x147
